# P0 x row loads tagged nt
# speedup vs baseline: 1.0263x; 1.0166x over previous
; __device__ __forceinline__ void rms_row_i8(const float* xrow, const float* gain, unsigned char* qrow, float* qscale, int lane) {
;     const f32x4* xr = (const f32x4*)xrow + lane; const f32x4* gr = (const f32x4*)gain + lane;
;     f32x4 v[16]; float s = 0.f;
; #pragma unroll
;     for (int j = 0; j < 16; ++j) { v[j] = xr[64 * j]; s += (v[j].x * v[j].x + v[j].y * v[j].y) + (v[j].z * v[j].z + v[j].w * v[j].w); }
; __device__ __forceinline__ void phase_prologue(const Frame& F, const Args& a) {
;     ...
;           for (int j = 0; j < 4; ++j) { const int m = m0 + 4 * F.wave + j; rms_row_i8(a.in[0] + (size_t)m * D, a.in[2], ws + WS_A + (size_t)m * D, (float*)(ws + SA_H) + m, F.lane); } } }
.LBB0_93:
	v_lshl_add_u64 v[46:47], v[98:99], 0, s[14:15]
	global_load_dwordx4 v[38:41], v[46:47], off nt
	global_load_dwordx4 v[30:33], v[46:47], off offset:1024 nt
	global_load_dwordx4 v[2:5], v[46:47], off offset:3072 nt
	global_load_dwordx4 v[18:21], v[46:47], off offset:2048 nt
	v_add_co_u32_e32 v116, vcc, s21, v46
	s_waitcnt vmcnt(2)
	v_pk_mul_f32 v[120:121], v[32:33], v[32:33]
	v_addc_co_u32_e32 v117, vcc, 0, v47, vcc
	global_load_dwordx4 v[6:9], v[116:117], off offset:-4096 nt
	v_add_co_u32_e32 v48, vcc, s20, v46
	v_pk_mul_f32 v[122:123], v[30:31], v[30:31]
	s_nop 0
	v_addc_co_u32_e32 v49, vcc, 0, v47, vcc
	global_load_dwordx4 v[10:13], v[48:49], off offset:2048 nt
	global_load_dwordx4 v[14:17], v[48:49], off offset:1024 nt
	global_load_dwordx4 v[26:29], v[48:49], off offset:3072 nt
	global_load_dwordx4 v[22:25], v[116:117], off offset:1024 nt
	global_load_dwordx4 v[34:37], v[116:117], off nt
	global_load_dwordx4 v[42:45], v[116:117], off offset:2048 nt
	v_add_co_u32_e32 v118, vcc, s22, v46
	s_waitcnt vmcnt(7)
	v_mul_f32_e32 v124, v19, v19
	v_addc_co_u32_e32 v119, vcc, 0, v47, vcc
	global_load_dwordx4 v[50:53], v[116:117], off offset:3072 nt
	global_load_dwordx4 v[46:49], v[118:119], off nt
	global_load_dwordx4 v[58:61], v[118:119], off offset:1024 nt
	global_load_dwordx4 v[62:65], v[118:119], off offset:2048 nt
	global_load_dwordx4 v[54:57], v[118:119], off offset:3072 nt
	v_pk_mul_f32 v[116:117], v[40:41], v[40:41]
	v_pk_mul_f32 v[118:119], v[38:39], v[38:39]
	v_mul_f32_e32 v126, v21, v21
	v_pk_mov_b32 v[128:129], v[118:119], v[116:117] op_sel:[1,0]
	v_mov_b32_e32 v119, v117
	v_pk_mov_b32 v[116:117], v[122:123], v[120:121] op_sel:[1,0]
	v_mov_b32_e32 v123, v121
	v_pk_add_f32 v[118:119], v[128:129], v[118:119]
	v_pk_add_f32 v[116:117], v[116:117], v[122:123]
	v_mul_f32_e32 v141, v2, v2
	v_mul_f32_e32 v142, v3, v3
	v_mul_f32_e32 v133, v4, v4
	v_mul_f32_e32 v135, v5, v5
	v_pk_fma_f32 v[120:121], v[18:19], v[18:19], v[124:125] op_sel_hi:[1,1,0]
	v_pk_fma_f32 v[124:125], v[20:21], v[20:21], v[126:127] op_sel_hi:[1,1,0]
	v_pk_add_f32 v[118:119], v[118:119], v[118:119] op_sel:[0,1] op_sel_hi:[1,0]
	v_pk_add_f32 v[116:117], v[116:117], v[116:117] op_sel:[0,1] op_sel_hi:[1,0]
	v_mov_b32_e32 v121, v133
	v_mov_b32_e32 v125, v135
	v_mov_b32_e32 v119, v141
	v_mov_b32_e32 v117, v142
	v_pk_add_f32 v[120:121], v[120:121], v[124:125]
	v_pk_add_f32 v[116:117], v[118:119], v[116:117]
	s_waitcnt vmcnt(11)
	v_pk_mul_f32 v[126:127], v[8:9], v[8:9]
	v_pk_mul_f32 v[130:131], v[6:7], v[6:7]
	s_waitcnt vmcnt(9)
	v_mul_f32_e32 v132, v15, v15
	v_pk_mov_b32 v[122:123], v[130:131], v[126:127] op_sel:[1,0]
	v_mov_b32_e32 v131, v127
	v_mul_f32_e32 v134, v17, v17
	v_pk_add_f32 v[122:123], v[122:123], v[130:131]
	v_pk_add_f32 v[116:117], v[116:117], v[120:121]
	v_mul_f32_e32 v143, v10, v10
	v_mul_f32_e32 v144, v11, v11
	v_mul_f32_e32 v145, v12, v12
	v_mul_f32_e32 v146, v13, v13
	v_pk_fma_f32 v[126:127], v[14:15], v[14:15], v[132:133] op_sel_hi:[1,1,0]
	v_pk_fma_f32 v[128:129], v[16:17], v[16:17], v[134:135] op_sel_hi:[1,1,0]
	v_pk_add_f32 v[122:123], v[122:123], v[122:123] op_sel:[0,1] op_sel_hi:[1,0]
	v_pk_add_f32 v[116:117], v[116:117], v[116:117] op_sel:[0,1] op_sel_hi:[1,0]
	s_waitcnt vmcnt(8)
	v_pk_mul_f32 v[136:137], v[28:29], v[28:29]
	v_pk_mul_f32 v[138:139], v[26:27], v[26:27]
	v_mov_b32_e32 v127, v145
	v_mov_b32_e32 v129, v146
	v_mov_b32_e32 v123, v144
	v_mov_b32_e32 v117, v143
	v_pk_mov_b32 v[132:133], v[138:139], v[136:137] op_sel:[1,0]
	v_mov_b32_e32 v139, v137
	v_pk_add_f32 v[126:127], v[126:127], v[128:129]
	v_pk_add_f32 v[116:117], v[116:117], v[122:123]
	s_waitcnt vmcnt(6)
	v_mul_f32_e32 v140, v35, v35
	v_pk_add_f32 v[124:125], v[132:133], v[138:139]
	v_pk_add_f32 v[116:117], v[116:117], v[126:127]
	v_mul_f32_e32 v118, v37, v37
	v_mul_f32_e32 v147, v22, v22
	v_mul_f32_e32 v148, v23, v23
	v_mul_f32_e32 v149, v24, v24
	v_mul_f32_e32 v150, v25, v25
	v_pk_fma_f32 v[134:135], v[34:35], v[34:35], v[140:141] op_sel_hi:[1,1,0]
	v_pk_add_f32 v[124:125], v[124:125], v[124:125] op_sel:[0,1] op_sel_hi:[1,0]
	v_pk_add_f32 v[116:117], v[116:117], v[116:117] op_sel:[0,1] op_sel_hi:[1,0]
	v_pk_fma_f32 v[118:119], v[36:37], v[36:37], v[118:119] op_sel_hi:[1,1,0]
	v_mov_b32_e32 v135, v149
	v_mov_b32_e32 v125, v148
	v_mov_b32_e32 v117, v147
	v_mov_b32_e32 v119, v150
	v_pk_add_f32 v[116:117], v[116:117], v[124:125]
	v_pk_add_f32 v[118:119], v[134:135], v[118:119]
	s_waitcnt vmcnt(5)
	v_pk_mul_f32 v[120:121], v[42:43], v[42:43]
	v_pk_add_f32 v[116:117], v[116:117], v[118:119]
	v_pk_mul_f32 v[118:119], v[44:45], v[44:45]
	v_pk_add_f32 v[116:117], v[116:117], v[116:117] op_sel:[0,1] op_sel_hi:[1,0]
	v_pk_mov_b32 v[122:123], v[120:121], v[118:119] op_sel:[1,0]
	v_mov_b32_e32 v121, v119
	v_pk_add_f32 v[118:119], v[122:123], v[120:121]
	s_waitcnt vmcnt(3)
	v_mul_f32_e32 v120, v46, v46
	v_mul_f32_e32 v121, v47, v47
	v_pk_add_f32 v[118:119], v[118:119], v[118:119] op_sel:[0,1] op_sel_hi:[1,0]
	v_mov_b32_e32 v117, v120
	v_mov_b32_e32 v119, v121
	v_pk_add_f32 v[116:117], v[116:117], v[118:119]
	v_mul_f32_e32 v118, v51, v51
	v_mul_f32_e32 v120, v53, v53
	v_mul_f32_e32 v122, v48, v48
	v_mul_f32_e32 v123, v49, v49
	v_pk_fma_f32 v[118:119], v[50:51], v[50:51], v[118:119] op_sel_hi:[1,1,0]
	v_pk_fma_f32 v[120:121], v[52:53], v[52:53], v[120:121] op_sel_hi:[1,1,0]
	v_mov_b32_e32 v119, v122
	v_mov_b32_e32 v121, v123
	v_pk_add_f32 v[118:119], v[118:119], v[120:121]
	s_waitcnt vmcnt(2)
	v_pk_mul_f32 v[120:121], v[58:59], v[58:59]
	v_pk_add_f32 v[116:117], v[116:117], v[118:119]
	v_pk_mul_f32 v[118:119], v[60:61], v[60:61]
	v_pk_add_f32 v[116:117], v[116:117], v[116:117] op_sel:[0,1] op_sel_hi:[1,0]
	v_pk_mov_b32 v[122:123], v[120:121], v[118:119] op_sel:[1,0]
	v_mov_b32_e32 v121, v119
	v_pk_add_f32 v[118:119], v[122:123], v[120:121]
	s_waitcnt vmcnt(0)
; __device__ __forceinline__ void rms_row_i8(const float* xrow, const float* gain, unsigned char* qrow, float* qscale, int lane) {
;     ...
;     for (int j = 0; j < 16; ++j) { v[j] = xr[64 * j]; s += (v[j].x * v[j].x + v[j].y * v[j].y) + (v[j].z * v[j].z + v[j].w * v[j].w); }
;     const float rstd = 1.f / sqrtf(wave_sum(s) * (1.f / D) + RMS_EPS);
;     float amax = 0.f;
; #pragma unroll
;     for (int j = 0; j < 16; ++j) { v[j] = v[j] * rstd * gr[64 * j]; amax = fmaxf(fmaxf(amax, fmaxf(fabsf(v[j].x), fabsf(v[j].y))), fmaxf(fabsf(v[j].z), fabsf(v[j].w))); }
	v_mul_f32_e32 v120, v54, v54
	v_mul_f32_e32 v121, v55, v55
	v_pk_add_f32 v[118:119], v[118:119], v[118:119] op_sel:[0,1] op_sel_hi:[1,0]
	v_mov_b32_e32 v117, v120
	v_mov_b32_e32 v119, v121
	v_pk_add_f32 v[116:117], v[116:117], v[118:119]
	v_mul_f32_e32 v118, v63, v63
	v_mul_f32_e32 v120, v65, v65
	v_mul_f32_e32 v122, v56, v56
	v_mul_f32_e32 v123, v57, v57
	v_pk_fma_f32 v[118:119], v[62:63], v[62:63], v[118:119] op_sel_hi:[1,1,0]
	v_pk_fma_f32 v[120:121], v[64:65], v[64:65], v[120:121] op_sel_hi:[1,1,0]
	v_mov_b32_e32 v119, v122
	v_mov_b32_e32 v121, v123
	v_pk_add_f32 v[118:119], v[118:119], v[120:121]
	global_load_dwordx4 v[140:143], v[76:77], off
	v_pk_add_f32 v[116:117], v[116:117], v[118:119]
	s_nop 0
	v_add_f32_e32 v120, v116, v117
	ds_bpermute_b32 v121, v110, v120
	global_load_dwordx4 v[116:119], v[70:71], off
	s_waitcnt lgkmcnt(0)
	v_add_f32_e32 v124, v120, v121
	ds_bpermute_b32 v125, v111, v124
	global_load_dwordx4 v[120:123], v[70:71], off offset:1024
	s_waitcnt lgkmcnt(0)
	v_add_f32_e32 v124, v124, v125
	ds_bpermute_b32 v125, v112, v124
	s_waitcnt lgkmcnt(0)
	v_add_f32_e32 v128, v124, v125
	global_load_dwordx4 v[124:127], v[70:71], off offset:2048
	ds_bpermute_b32 v129, v113, v128
	s_waitcnt lgkmcnt(0)
	v_add_f32_e32 v132, v128, v129
	ds_bpermute_b32 v133, v114, v132
	global_load_dwordx4 v[128:131], v[70:71], off offset:3072
	s_waitcnt lgkmcnt(0)
	v_add_f32_e32 v136, v132, v133
	ds_bpermute_b32 v137, v115, v136
	global_load_dwordx4 v[132:135], v[72:73], off
	s_waitcnt lgkmcnt(0)
	v_add_f32_e32 v136, v136, v137
	v_fmamk_f32 v136, v136, 0x39800000, v108
	v_mul_f32_e32 v137, 0x4f800000, v136
	v_cmp_gt_f32_e32 vcc, s23, v136
	s_nop 1
	v_cndmask_b32_e32 v148, v136, v137, vcc
	v_sqrt_f32_e32 v144, v148
	global_load_dwordx4 v[136:139], v[74:75], off
	v_add_u32_e32 v145, -1, v144
	v_fma_f32 v146, -v145, v144, v148
	v_cmp_ge_f32_e64 s[8:9], 0, v146
	v_add_u32_e32 v146, 1, v144
	s_nop 0
	v_cndmask_b32_e64 v145, v144, v145, s[8:9]
	v_fma_f32 v144, -v146, v144, v148
	v_cmp_lt_f32_e64 s[8:9], 0, v144
	s_nop 1
	v_cndmask_b32_e64 v149, v145, v146, s[8:9]
	v_mul_f32_e32 v150, 0x37800000, v149
	v_cndmask_b32_e32 v149, v149, v150, vcc
	v_cmp_class_f32_e32 vcc, v148, v109
	global_load_dwordx4 v[144:147], v[78:79], off
	s_nop 0
	v_cndmask_b32_e32 v160, v149, v148, vcc
	v_div_scale_f32 v156, s[8:9], v160, v160, 1.0
	v_rcp_f32_e32 v161, v156
	global_load_dwordx4 v[148:151], v[80:81], off
	v_div_scale_f32 v157, vcc, 1.0, v160, 1.0
	v_fma_f32 v152, -v156, v161, 1.0
	v_fmac_f32_e32 v161, v152, v161
	v_mul_f32_e32 v162, v157, v161
	global_load_dwordx4 v[152:155], v[82:83], off
	v_fma_f32 v158, -v156, v162, v157
	v_fmac_f32_e32 v162, v158, v161
	v_fma_f32 v163, -v156, v162, v157
	global_load_dwordx4 v[156:159], v[84:85], off
	v_div_fmas_f32 v161, v163, v161, v162
	v_div_fixup_f32 v160, v161, v160, 1.0
	v_pk_mul_f32 v[38:39], v[38:39], v[160:161] op_sel_hi:[1,0]
	v_pk_mul_f32 v[40:41], v[40:41], v[160:161] op_sel_hi:[1,0]
	s_waitcnt vmcnt(9)
	v_pk_mul_f32 v[164:165], v[116:117], v[38:39]
	v_pk_mul_f32 v[162:163], v[118:119], v[40:41]
	global_load_dwordx4 v[38:41], v[86:87], off
	v_max_f32_e64 v116, |v164|, |v165|
	v_max_f32_e64 v117, |v162|, |v163|
	v_max3_f32 v118, v116, 0, v117
	v_pk_mul_f32 v[116:117], v[30:31], v[160:161] op_sel_hi:[1,0]
	v_pk_mul_f32 v[30:31], v[32:33], v[160:161] op_sel_hi:[1,0]
	s_waitcnt vmcnt(9)
	v_pk_mul_f32 v[168:169], v[120:121], v[116:117]
	v_pk_mul_f32 v[166:167], v[122:123], v[30:31]
	global_load_dwordx4 v[30:33], v[88:89], off
	v_max_f32_e64 v116, |v168|, |v169|
	v_max_f32_e64 v117, |v166|, |v167|
	v_max3_f32 v120, v118, v116, v117
	v_pk_mul_f32 v[18:19], v[18:19], v[160:161] op_sel_hi:[1,0]
	v_pk_mul_f32 v[20:21], v[20:21], v[160:161] op_sel_hi:[1,0]
	global_load_dwordx4 v[116:119], v[90:91], off
	s_waitcnt vmcnt(10)
	v_pk_mul_f32 v[170:171], v[126:127], v[20:21]
	v_pk_mul_f32 v[172:173], v[124:125], v[18:19]
	v_max_f32_e64 v19, |v170|, |v171|
	v_max_f32_e64 v18, |v172|, |v173|
	v_max3_f32 v18, v120, v18, v19
	global_load_dwordx4 v[120:123], v[92:93], off
	global_load_dwordx4 v[124:127], v[94:95], off
	v_pk_mul_f32 v[2:3], v[2:3], v[160:161] op_sel_hi:[1,0]
	v_pk_mul_f32 v[4:5], v[4:5], v[160:161] op_sel_hi:[1,0]
	s_waitcnt vmcnt(11)
	v_pk_mul_f32 v[128:129], v[128:129], v[2:3]
	v_pk_mul_f32 v[130:131], v[130:131], v[4:5]
	v_max_f32_e64 v2, |v128|, |v129|
	v_max_f32_e64 v3, |v130|, |v131|
	v_max3_f32 v18, v18, v2, v3
	v_pk_mul_f32 v[2:3], v[6:7], v[160:161] op_sel_hi:[1,0]
	v_pk_mul_f32 v[4:5], v[8:9], v[160:161] op_sel_hi:[1,0]
	s_waitcnt vmcnt(10)
	v_pk_mul_f32 v[132:133], v[132:133], v[2:3]
	v_pk_mul_f32 v[134:135], v[134:135], v[4:5]
	v_max_f32_e64 v2, |v132|, |v133|
	v_max_f32_e64 v3, |v134|, |v135|
	v_max3_f32 v6, v18, v2, v3
	v_pk_mul_f32 v[2:3], v[14:15], v[160:161] op_sel_hi:[1,0]
	v_pk_mul_f32 v[4:5], v[16:17], v[160:161] op_sel_hi:[1,0]
	s_waitcnt vmcnt(9)
	v_pk_mul_f32 v[136:137], v[136:137], v[2:3]
	v_pk_mul_f32 v[138:139], v[138:139], v[4:5]
	v_max_f32_e64 v2, |v136|, |v137|
	v_max_f32_e64 v3, |v138|, |v139|
	v_max3_f32 v6, v6, v2, v3
	v_pk_mul_f32 v[2:3], v[10:11], v[160:161] op_sel_hi:[1,0]
	v_pk_mul_f32 v[4:5], v[12:13], v[160:161] op_sel_hi:[1,0]
	v_pk_mul_f32 v[140:141], v[140:141], v[2:3]
	v_pk_mul_f32 v[142:143], v[142:143], v[4:5]
	v_max_f32_e64 v2, |v140|, |v141|
	v_max_f32_e64 v3, |v142|, |v143|
	v_max3_f32 v6, v6, v2, v3
	v_pk_mul_f32 v[2:3], v[26:27], v[160:161] op_sel_hi:[1,0]
	v_pk_mul_f32 v[4:5], v[28:29], v[160:161] op_sel_hi:[1,0]
	s_waitcnt vmcnt(8)
; __device__ __forceinline__ void rms_row_i8(const float* xrow, const float* gain, unsigned char* qrow, float* qscale, int lane) {
;     ...
;     for (int j = 0; j < 16; ++j) { v[j] = v[j] * rstd * gr[64 * j]; amax = fmaxf(fmaxf(amax, fmaxf(fabsf(v[j].x), fabsf(v[j].y))), fmaxf(fabsf(v[j].z), fabsf(v[j].w))); }
; #pragma unroll
;     for (int o = 1; o < 64; o <<= 1) amax = fmaxf(amax, __shfl_xor(amax, o));
;     const float scale = amax > 0.f ? 127.f / amax : 0.f;
; #pragma unroll
;     for (int j = 0; j < 16; ++j) ((unsigned*)qrow)[lane + 64 * j] = pack_i8x4(v[j].x * scale, v[j].y * scale, v[j].z * scale, v[j].w * scale);
	v_pk_mul_f32 v[144:145], v[144:145], v[2:3]
	v_pk_mul_f32 v[146:147], v[146:147], v[4:5]
	v_max_f32_e64 v2, |v144|, |v145|
	v_max_f32_e64 v3, |v146|, |v147|
	v_max3_f32 v6, v6, v2, v3
	v_pk_mul_f32 v[2:3], v[34:35], v[160:161] op_sel_hi:[1,0]
	v_pk_mul_f32 v[4:5], v[36:37], v[160:161] op_sel_hi:[1,0]
	s_waitcnt vmcnt(7)
	v_pk_mul_f32 v[36:37], v[148:149], v[2:3]
	v_pk_mul_f32 v[34:35], v[150:151], v[4:5]
	v_max_f32_e64 v2, |v36|, |v37|
	v_max_f32_e64 v3, |v34|, |v35|
	v_max3_f32 v6, v6, v2, v3
	v_pk_mul_f32 v[2:3], v[22:23], v[160:161] op_sel_hi:[1,0]
	v_pk_mul_f32 v[4:5], v[24:25], v[160:161] op_sel_hi:[1,0]
	s_waitcnt vmcnt(6)
	v_pk_mul_f32 v[150:151], v[152:153], v[2:3]
	v_pk_mul_f32 v[148:149], v[154:155], v[4:5]
	v_max_f32_e64 v2, |v150|, |v151|
	v_max_f32_e64 v3, |v148|, |v149|
	v_max3_f32 v6, v6, v2, v3
	v_pk_mul_f32 v[2:3], v[42:43], v[160:161] op_sel_hi:[1,0]
	v_pk_mul_f32 v[4:5], v[44:45], v[160:161] op_sel_hi:[1,0]
	s_waitcnt vmcnt(5)
	v_pk_mul_f32 v[26:27], v[156:157], v[2:3]
	v_pk_mul_f32 v[24:25], v[158:159], v[4:5]
	v_max_f32_e64 v2, |v26|, |v27|
	v_max_f32_e64 v3, |v24|, |v25|
	v_max3_f32 v6, v6, v2, v3
	v_pk_mul_f32 v[2:3], v[50:51], v[160:161] op_sel_hi:[1,0]
	v_pk_mul_f32 v[4:5], v[52:53], v[160:161] op_sel_hi:[1,0]
	s_waitcnt vmcnt(4)
	v_pk_mul_f32 v[22:23], v[2:3], v[38:39]
	v_pk_mul_f32 v[18:19], v[4:5], v[40:41]
	v_max_f32_e64 v2, |v22|, |v23|
	v_max_f32_e64 v3, |v18|, |v19|
	v_max3_f32 v6, v6, v2, v3
	v_pk_mul_f32 v[2:3], v[46:47], v[160:161] op_sel_hi:[1,0]
	v_pk_mul_f32 v[4:5], v[48:49], v[160:161] op_sel_hi:[1,0]
	s_waitcnt vmcnt(3)
	v_pk_mul_f32 v[16:17], v[2:3], v[30:31]
	v_pk_mul_f32 v[14:15], v[4:5], v[32:33]
	v_max_f32_e64 v2, |v16|, |v17|
	v_max_f32_e64 v3, |v14|, |v15|
	v_max3_f32 v6, v6, v2, v3
	v_pk_mul_f32 v[2:3], v[58:59], v[160:161] op_sel_hi:[1,0]
	v_pk_mul_f32 v[4:5], v[60:61], v[160:161] op_sel_hi:[1,0]
	s_waitcnt vmcnt(2)
	v_pk_mul_f32 v[12:13], v[2:3], v[116:117]
	v_pk_mul_f32 v[10:11], v[4:5], v[118:119]
	v_max_f32_e64 v2, |v12|, |v13|
	v_max_f32_e64 v3, |v10|, |v11|
	v_max3_f32 v20, v6, v2, v3
	v_pk_mul_f32 v[2:3], v[62:63], v[160:161] op_sel_hi:[1,0]
	v_pk_mul_f32 v[4:5], v[64:65], v[160:161] op_sel_hi:[1,0]
	s_waitcnt vmcnt(1)
	v_pk_mul_f32 v[8:9], v[2:3], v[120:121]
	v_pk_mul_f32 v[6:7], v[4:5], v[122:123]
	v_max_f32_e64 v2, |v8|, |v9|
	v_max_f32_e64 v3, |v6|, |v7|
	v_max3_f32 v20, v20, v2, v3
	v_pk_mul_f32 v[4:5], v[54:55], v[160:161] op_sel_hi:[1,0]
	v_pk_mul_f32 v[2:3], v[56:57], v[160:161] op_sel_hi:[1,0]
	s_waitcnt vmcnt(0)
	v_pk_mul_f32 v[4:5], v[4:5], v[124:125]
	v_pk_mul_f32 v[2:3], v[2:3], v[126:127]
	v_max_f32_e64 v21, |v4|, |v5|
	v_max_f32_e64 v28, |v2|, |v3|
	v_max3_f32 v20, v20, v21, v28
	ds_bpermute_b32 v21, v110, v20
	s_waitcnt lgkmcnt(0)
	v_max_f32_e32 v21, v21, v21
	v_max_f32_e32 v20, v20, v21
	ds_bpermute_b32 v21, v111, v20
	s_waitcnt lgkmcnt(0)
	v_max_f32_e32 v21, v21, v21
	v_max_f32_e32 v20, v20, v21
	ds_bpermute_b32 v21, v112, v20
	s_waitcnt lgkmcnt(0)
	v_max_f32_e32 v21, v21, v21
	v_max_f32_e32 v20, v20, v21
	ds_bpermute_b32 v21, v113, v20
	s_waitcnt lgkmcnt(0)
	v_max_f32_e32 v21, v21, v21
	v_max_f32_e32 v20, v20, v21
	ds_bpermute_b32 v21, v114, v20
	s_waitcnt lgkmcnt(0)
	v_max_f32_e32 v21, v21, v21
	v_max_f32_e32 v20, v20, v21
	ds_bpermute_b32 v21, v115, v20
	s_waitcnt lgkmcnt(0)
	v_max_f32_e32 v21, v21, v21
	v_max_f32_e32 v28, v20, v21
	v_div_scale_f32 v20, s[8:9], v28, v28, s24
	v_rcp_f32_e32 v21, v20
	s_nop 0
	v_fma_f32 v29, -v20, v21, 1.0
	v_fmac_f32_e32 v21, v29, v21
	v_div_scale_f32 v29, vcc, s24, v28, s24
	v_mul_f32_e32 v30, v29, v21
	v_fma_f32 v31, -v20, v30, v29
	v_fmac_f32_e32 v30, v31, v21
	v_fma_f32 v20, -v20, v30, v29
	v_div_fmas_f32 v20, v20, v21, v30
	v_div_fixup_f32 v20, v20, v28, s24
	v_cmp_lt_f32_e32 vcc, 0, v28
	s_nop 1
	v_cndmask_b32_e32 v29, 0, v20, vcc
	v_mul_f32_e32 v21, v165, v29
	v_mul_f32_e32 v20, v164, v29
	v_mul_f32_e32 v30, v162, v29
	v_mul_f32_e32 v31, v163, v29
	v_rndne_f32_e32 v21, v21
	v_rndne_f32_e32 v20, v20
	v_cvt_i32_f32_e32 v21, v21
	v_rndne_f32_e32 v30, v30
	v_rndne_f32_e32 v31, v31
	v_cvt_i32_f32_e32 v20, v20
	v_cvt_i32_f32_sdwa v30, v30 dst_sel:WORD_1 dst_unused:UNUSED_PAD src0_sel:DWORD
	v_cvt_i32_f32_e32 v31, v31
	v_lshlrev_b32_e32 v21, 8, v21
	v_and_b32_e32 v21, 0xff00, v21
	v_and_b32_e32 v30, 0xff0000, v30
	v_perm_b32 v20, v31, v20, s25
	v_or3_b32 v30, v20, v21, v30
	v_lshl_add_u64 v[20:21], s[4:5], 0, v[100:101]
	v_add_co_u32_e32 v20, vcc, s26, v20
	v_mul_f32_e32 v31, v169, v29
	s_nop 0
	v_addc_co_u32_e32 v21, vcc, 0, v21, vcc
	global_store_dword v[20:21], v30, off
	v_mul_f32_e32 v30, v168, v29
	v_mul_f32_e32 v32, v166, v29
	v_mul_f32_e32 v33, v167, v29
	v_rndne_f32_e32 v31, v31
	v_rndne_f32_e32 v30, v30
	v_cvt_i32_f32_e32 v31, v31
	v_rndne_f32_e32 v32, v32
	v_rndne_f32_e32 v33, v33
	v_cvt_i32_f32_e32 v30, v30
	v_cvt_i32_f32_sdwa v32, v32 dst_sel:WORD_1 dst_unused:UNUSED_PAD src0_sel:DWORD
	v_cvt_i32_f32_e32 v33, v33
	v_lshlrev_b32_e32 v31, 8, v31
	v_and_b32_e32 v31, 0xff00, v31
	v_and_b32_e32 v32, 0xff0000, v32
	v_perm_b32 v30, v33, v30, s25
	v_or3_b32 v30, v30, v31, v32
	v_mul_f32_e32 v31, v173, v29
	global_store_dword v[20:21], v30, off offset:256
	v_mul_f32_e32 v30, v172, v29
	v_mul_f32_e32 v32, v170, v29
	v_mul_f32_e32 v33, v171, v29
	v_rndne_f32_e32 v31, v31
	v_rndne_f32_e32 v30, v30
	v_cvt_i32_f32_e32 v31, v31
	v_rndne_f32_e32 v32, v32
	v_rndne_f32_e32 v33, v33
	v_cvt_i32_f32_e32 v30, v30
	v_cvt_i32_f32_sdwa v32, v32 dst_sel:WORD_1 dst_unused:UNUSED_PAD src0_sel:DWORD
	v_cvt_i32_f32_e32 v33, v33
	v_lshlrev_b32_e32 v31, 8, v31
	v_and_b32_e32 v31, 0xff00, v31
	v_and_b32_e32 v32, 0xff0000, v32
	v_perm_b32 v30, v33, v30, s25
; __device__ __forceinline__ void rms_row_i8(const float* xrow, const float* gain, unsigned char* qrow, float* qscale, int lane) {
;     ...
; #pragma unroll
;     for (int j = 0; j < 16; ++j) ((unsigned*)qrow)[lane + 64 * j] = pack_i8x4(v[j].x * scale, v[j].y * scale, v[j].z * scale, v[j].w * scale);
	v_or3_b32 v30, v30, v31, v32
	v_mul_f32_e32 v31, v129, v29
	global_store_dword v[20:21], v30, off offset:512
	v_mul_f32_e32 v30, v128, v29
	v_mul_f32_e32 v32, v130, v29
	v_mul_f32_e32 v33, v131, v29
	v_rndne_f32_e32 v31, v31
	v_rndne_f32_e32 v30, v30
	v_cvt_i32_f32_e32 v31, v31
	v_rndne_f32_e32 v32, v32
	v_rndne_f32_e32 v33, v33
	v_cvt_i32_f32_e32 v30, v30
	v_cvt_i32_f32_sdwa v32, v32 dst_sel:WORD_1 dst_unused:UNUSED_PAD src0_sel:DWORD
	v_cvt_i32_f32_e32 v33, v33
	v_lshlrev_b32_e32 v31, 8, v31
	v_and_b32_e32 v31, 0xff00, v31
	v_and_b32_e32 v32, 0xff0000, v32
	v_perm_b32 v30, v33, v30, s25
	v_or3_b32 v30, v30, v31, v32
	v_mul_f32_e32 v31, v133, v29
	global_store_dword v[20:21], v30, off offset:768
	v_mul_f32_e32 v30, v132, v29
	v_mul_f32_e32 v32, v134, v29
	v_mul_f32_e32 v33, v135, v29
	v_rndne_f32_e32 v31, v31
	v_rndne_f32_e32 v30, v30
	v_cvt_i32_f32_e32 v31, v31
	v_rndne_f32_e32 v32, v32
	v_rndne_f32_e32 v33, v33
	v_cvt_i32_f32_e32 v30, v30
	v_cvt_i32_f32_sdwa v32, v32 dst_sel:WORD_1 dst_unused:UNUSED_PAD src0_sel:DWORD
	v_cvt_i32_f32_e32 v33, v33
	v_lshlrev_b32_e32 v31, 8, v31
	v_and_b32_e32 v31, 0xff00, v31
	v_and_b32_e32 v32, 0xff0000, v32
	v_perm_b32 v30, v33, v30, s25
	v_or3_b32 v30, v30, v31, v32
	v_mul_f32_e32 v31, v137, v29
	global_store_dword v[20:21], v30, off offset:1024
	v_mul_f32_e32 v30, v136, v29
	v_mul_f32_e32 v32, v138, v29
	v_mul_f32_e32 v33, v139, v29
	v_rndne_f32_e32 v31, v31
	v_rndne_f32_e32 v30, v30
	v_cvt_i32_f32_e32 v31, v31
	v_rndne_f32_e32 v32, v32
	v_rndne_f32_e32 v33, v33
	v_cvt_i32_f32_e32 v30, v30
	v_cvt_i32_f32_sdwa v32, v32 dst_sel:WORD_1 dst_unused:UNUSED_PAD src0_sel:DWORD
	v_cvt_i32_f32_e32 v33, v33
	v_lshlrev_b32_e32 v31, 8, v31
	v_and_b32_e32 v31, 0xff00, v31
	v_and_b32_e32 v32, 0xff0000, v32
	v_perm_b32 v30, v33, v30, s25
	v_or3_b32 v30, v30, v31, v32
	v_mul_f32_e32 v31, v141, v29
	global_store_dword v[20:21], v30, off offset:1280
	v_mul_f32_e32 v30, v140, v29
	v_mul_f32_e32 v32, v142, v29
	v_mul_f32_e32 v33, v143, v29
	v_rndne_f32_e32 v31, v31
	v_rndne_f32_e32 v30, v30
	v_cvt_i32_f32_e32 v31, v31
	v_rndne_f32_e32 v32, v32
	v_rndne_f32_e32 v33, v33
	v_cvt_i32_f32_e32 v30, v30
	v_cvt_i32_f32_sdwa v32, v32 dst_sel:WORD_1 dst_unused:UNUSED_PAD src0_sel:DWORD
	v_cvt_i32_f32_e32 v33, v33
	v_lshlrev_b32_e32 v31, 8, v31
	v_and_b32_e32 v31, 0xff00, v31
	v_and_b32_e32 v32, 0xff0000, v32
	v_perm_b32 v30, v33, v30, s25
	v_or3_b32 v30, v30, v31, v32
	v_mul_f32_e32 v31, v145, v29
	global_store_dword v[20:21], v30, off offset:1536
	v_mul_f32_e32 v30, v144, v29
	v_mul_f32_e32 v32, v146, v29
	v_mul_f32_e32 v33, v147, v29
	v_rndne_f32_e32 v31, v31
	v_rndne_f32_e32 v30, v30
	v_cvt_i32_f32_e32 v31, v31
	v_rndne_f32_e32 v32, v32
	v_rndne_f32_e32 v33, v33
	v_cvt_i32_f32_e32 v30, v30
	v_cvt_i32_f32_sdwa v32, v32 dst_sel:WORD_1 dst_unused:UNUSED_PAD src0_sel:DWORD
	v_cvt_i32_f32_e32 v33, v33
	v_lshlrev_b32_e32 v31, 8, v31
	v_and_b32_e32 v31, 0xff00, v31
	v_and_b32_e32 v32, 0xff0000, v32
	v_perm_b32 v30, v33, v30, s25
	v_or3_b32 v30, v30, v31, v32
	v_mul_f32_e32 v31, v37, v29
	global_store_dword v[20:21], v30, off offset:1792
	v_mul_f32_e32 v30, v36, v29
	v_mul_f32_e32 v32, v34, v29
	v_mul_f32_e32 v33, v35, v29
	v_rndne_f32_e32 v31, v31
	v_rndne_f32_e32 v30, v30
	v_cvt_i32_f32_e32 v31, v31
	v_rndne_f32_e32 v32, v32
	v_rndne_f32_e32 v33, v33
	v_cvt_i32_f32_e32 v30, v30
	v_cvt_i32_f32_sdwa v32, v32 dst_sel:WORD_1 dst_unused:UNUSED_PAD src0_sel:DWORD
	v_cvt_i32_f32_e32 v33, v33
	v_lshlrev_b32_e32 v31, 8, v31
	v_and_b32_e32 v31, 0xff00, v31
	v_and_b32_e32 v32, 0xff0000, v32
	v_perm_b32 v30, v33, v30, s25
	v_or3_b32 v30, v30, v31, v32
	v_mul_f32_e32 v31, v151, v29
	v_mul_f32_e32 v27, v27, v29
	v_mul_f32_e32 v23, v23, v29
	v_mul_f32_e32 v17, v17, v29
	v_mul_f32_e32 v13, v13, v29
	v_mul_f32_e32 v9, v9, v29
	v_mul_f32_e32 v5, v5, v29
	global_store_dword v[20:21], v30, off offset:2048
	v_mul_f32_e32 v30, v150, v29
	v_mul_f32_e32 v32, v148, v29
	v_mul_f32_e32 v33, v149, v29
	v_rndne_f32_e32 v31, v31
; __device__ __forceinline__ void rms_row_i8(const float* xrow, const float* gain, unsigned char* qrow, float* qscale, int lane) {
;     ...
; #pragma unroll
;     for (int j = 0; j < 16; ++j) ((unsigned*)qrow)[lane + 64 * j] = pack_i8x4(v[j].x * scale, v[j].y * scale, v[j].z * scale, v[j].w * scale);
;     if (lane == 0) *qscale = amax * (1.f / 127.f);
	v_mul_f32_e32 v26, v26, v29
	v_mul_f32_e32 v24, v24, v29
	v_mul_f32_e32 v25, v25, v29
	v_rndne_f32_e32 v27, v27
	v_mul_f32_e32 v22, v22, v29
	v_mul_f32_e32 v18, v18, v29
	v_mul_f32_e32 v19, v19, v29
	v_rndne_f32_e32 v23, v23
	v_mul_f32_e32 v16, v16, v29
	v_mul_f32_e32 v14, v14, v29
	v_mul_f32_e32 v15, v15, v29
	v_rndne_f32_e32 v17, v17
	v_mul_f32_e32 v12, v12, v29
	v_mul_f32_e32 v10, v10, v29
	v_mul_f32_e32 v11, v11, v29
	v_rndne_f32_e32 v13, v13
	v_mul_f32_e32 v8, v8, v29
	v_mul_f32_e32 v6, v6, v29
	v_mul_f32_e32 v7, v7, v29
	v_rndne_f32_e32 v9, v9
	v_mul_f32_e32 v4, v4, v29
	v_mul_f32_e32 v2, v2, v29
	v_mul_f32_e32 v3, v3, v29
	v_rndne_f32_e32 v5, v5
	v_rndne_f32_e32 v30, v30
	v_cvt_i32_f32_e32 v31, v31
	v_rndne_f32_e32 v32, v32
	v_rndne_f32_e32 v33, v33
	v_rndne_f32_e32 v26, v26
	v_cvt_i32_f32_e32 v27, v27
	v_rndne_f32_e32 v24, v24
	v_rndne_f32_e32 v25, v25
	v_rndne_f32_e32 v22, v22
	v_cvt_i32_f32_e32 v23, v23
	v_rndne_f32_e32 v18, v18
	v_rndne_f32_e32 v19, v19
	v_rndne_f32_e32 v16, v16
	v_cvt_i32_f32_e32 v17, v17
	v_rndne_f32_e32 v14, v14
	v_rndne_f32_e32 v15, v15
	v_rndne_f32_e32 v12, v12
	v_cvt_i32_f32_e32 v13, v13
	v_rndne_f32_e32 v10, v10
	v_rndne_f32_e32 v11, v11
	v_rndne_f32_e32 v8, v8
	v_cvt_i32_f32_e32 v9, v9
	v_rndne_f32_e32 v6, v6
	v_rndne_f32_e32 v7, v7
	v_rndne_f32_e32 v4, v4
	v_cvt_i32_f32_e32 v5, v5
	v_rndne_f32_e32 v2, v2
	v_rndne_f32_e32 v3, v3
	v_cvt_i32_f32_e32 v30, v30
	v_cvt_i32_f32_sdwa v32, v32 dst_sel:WORD_1 dst_unused:UNUSED_PAD src0_sel:DWORD
	v_cvt_i32_f32_e32 v33, v33
	v_cvt_i32_f32_e32 v26, v26
	v_cvt_i32_f32_sdwa v24, v24 dst_sel:WORD_1 dst_unused:UNUSED_PAD src0_sel:DWORD
	v_cvt_i32_f32_e32 v25, v25
	v_cvt_i32_f32_e32 v22, v22
	v_cvt_i32_f32_sdwa v18, v18 dst_sel:WORD_1 dst_unused:UNUSED_PAD src0_sel:DWORD
	v_cvt_i32_f32_e32 v19, v19
	v_cvt_i32_f32_e32 v16, v16
	v_cvt_i32_f32_sdwa v14, v14 dst_sel:WORD_1 dst_unused:UNUSED_PAD src0_sel:DWORD
	v_cvt_i32_f32_e32 v15, v15
	v_cvt_i32_f32_e32 v12, v12
	v_cvt_i32_f32_sdwa v10, v10 dst_sel:WORD_1 dst_unused:UNUSED_PAD src0_sel:DWORD
	v_cvt_i32_f32_e32 v11, v11
	v_cvt_i32_f32_e32 v8, v8
	v_cvt_i32_f32_sdwa v6, v6 dst_sel:WORD_1 dst_unused:UNUSED_PAD src0_sel:DWORD
	v_cvt_i32_f32_e32 v7, v7
	v_cvt_i32_f32_e32 v4, v4
	v_cvt_i32_f32_sdwa v2, v2 dst_sel:WORD_1 dst_unused:UNUSED_PAD src0_sel:DWORD
	v_cvt_i32_f32_e32 v3, v3
	v_lshlrev_b32_e32 v31, 8, v31
	v_lshlrev_b32_e32 v27, 8, v27
	v_lshlrev_b32_e32 v23, 8, v23
	v_lshlrev_b32_e32 v17, 8, v17
	v_lshlrev_b32_e32 v13, 8, v13
	v_lshlrev_b32_e32 v9, 8, v9
	v_lshlrev_b32_e32 v5, 8, v5
	v_and_b32_e32 v31, 0xff00, v31
	v_and_b32_e32 v32, 0xff0000, v32
	v_perm_b32 v30, v33, v30, s25
	v_and_b32_e32 v27, 0xff00, v27
	v_and_b32_e32 v24, 0xff0000, v24
	v_perm_b32 v25, v25, v26, s25
	v_and_b32_e32 v23, 0xff00, v23
	v_and_b32_e32 v18, 0xff0000, v18
	v_perm_b32 v19, v19, v22, s25
	v_and_b32_e32 v17, 0xff00, v17
	v_and_b32_e32 v14, 0xff0000, v14
	v_perm_b32 v15, v15, v16, s25
	v_and_b32_e32 v13, 0xff00, v13
	v_and_b32_e32 v10, 0xff0000, v10
	v_perm_b32 v11, v11, v12, s25
	v_and_b32_e32 v9, 0xff00, v9
	v_and_b32_e32 v6, 0xff0000, v6
	v_perm_b32 v7, v7, v8, s25
	v_and_b32_e32 v5, 0xff00, v5
	v_and_b32_e32 v2, 0xff0000, v2
	v_perm_b32 v3, v3, v4, s25
	v_or3_b32 v30, v30, v31, v32
	v_or3_b32 v24, v25, v27, v24
	v_or3_b32 v18, v19, v23, v18
	v_or3_b32 v14, v15, v17, v14
	v_or3_b32 v10, v11, v13, v10
	v_or3_b32 v6, v7, v9, v6
	v_or3_b32 v2, v3, v5, v2
	global_store_dword v[20:21], v30, off offset:2304
	global_store_dword v[20:21], v24, off offset:2560
	global_store_dword v[20:21], v18, off offset:2816
	global_store_dword v[20:21], v14, off offset:3072
	global_store_dword v[20:21], v10, off offset:3328
	global_store_dword v[20:21], v6, off offset:3584
	global_store_dword v[20:21], v2, off offset:3840
	s_and_saveexec_b64 s[8:9], s[6:7]
	s_cbranch_execz .LBB0_92
	s_add_u32 s28, s4, s16
	s_addc_u32 s29, s5, s17
	v_mul_f32_e32 v2, 0x3c010204, v28
	global_store_dword v69, v2, s[28:29]
	s_branch .LBB0_92
